# code placement: 32-byte pad before the MoE K-loop preheader
# speedup vs baseline: 1.0068x; 1.0068x over previous
.Lmoe_rows_direct:
	v_mov_b32_e32 v248, v134
	v_mov_b32_e32 v249, v136
	v_mov_b32_e32 v250, v138
	v_mov_b32_e32 v223, v140
	s_nop 0
	s_nop 0
	s_nop 0
	s_nop 0
	s_nop 0
	s_nop 0
	s_nop 0
	s_nop 0
